# K1 epilogue: c2p pointer load hoisted to kernel entry; split-K partial and c2 stores made write-through (sc0 sc1)
# speedup vs baseline: 1.0459x; 1.0459x over previous
.LBB0_4:
	s_load_dwordx2 s[12:13], s[0:1], 0x10
	s_load_dwordx4 s[20:23], s[0:1], 0x0
	s_load_dwordx2 s[24:25], s[0:1], 0x18
	v_lshrrev_b32_e32 v1, 6, v0
	v_and_b32_e32 v130, 15, v0
	v_cmp_le_u32_e32 vcc, s4, v1
	s_and_saveexec_b64 s[4:5], vcc
	s_xor_b64 s[4:5], exec, s[4:5]
	s_cbranch_execz .LBB0_6
	v_lshlrev_b32_e32 v2, 2, v130
	v_lshl_or_b32 v2, v1, 10, v2
	v_or_b32_e32 v3, 0x20000, v2
	v_mov_b32_e32 v4, 0
	ds_write_b32 v3, v4
	v_or_b32_e32 v3, 0x20200, v2
	ds_write_b32 v3, v4
	v_or_b32_e32 v3, 0x20040, v2
	ds_write_b32 v3, v4
	v_or_b32_e32 v3, 0x20240, v2
	ds_write_b32 v3, v4
	v_or_b32_e32 v3, 0x20080, v2
	ds_write_b32 v3, v4
	v_or_b32_e32 v3, 0x20280, v2
	ds_write_b32 v3, v4
	v_or_b32_e32 v3, 0x200c0, v2
	ds_write_b32 v3, v4
	v_or_b32_e32 v3, 0x202c0, v2
	ds_write_b32 v3, v4
	v_or_b32_e32 v3, 0x20100, v2
	ds_write_b32 v3, v4
	v_or_b32_e32 v3, 0x20300, v2
	ds_write_b32 v3, v4
	v_or_b32_e32 v3, 0x20140, v2
	ds_write_b32 v3, v4
	v_or_b32_e32 v3, 0x20340, v2
	ds_write_b32 v3, v4
	v_or_b32_e32 v3, 0x20180, v2
	ds_write_b32 v3, v4
	v_or_b32_e32 v3, 0x20380, v2
	ds_write_b32 v3, v4
	v_or_b32_e32 v3, 0x201c0, v2
	v_or_b32_e32 v2, 0x203c0, v2
	ds_write_b32 v3, v4
	ds_write_b32 v2, v4

.LBB0_8:
	s_or_b64 exec, exec, s[14:15]
	v_lshlrev_b32_e32 v10, 4, v194
	v_lshl_or_b32 v1, v1, 14, v10
	v_lshlrev_b32_e32 v194, 4, v0
	s_waitcnt lgkmcnt(0)
	s_barrier
	ds_write_b128 v1, v[58:61]
	ds_write_b128 v1, v[62:65] offset:1024
	ds_write_b128 v1, v[74:77] offset:2048
	ds_write_b128 v1, v[78:81] offset:3072
	ds_write_b128 v1, v[82:85] offset:4096
	ds_write_b128 v1, v[86:89] offset:5120
	ds_write_b128 v1, v[90:93] offset:6144
	ds_write_b128 v1, v[94:97] offset:7168
	ds_write_b128 v1, v[98:101] offset:8192
	ds_write_b128 v1, v[102:105] offset:9216
	ds_write_b128 v1, v[106:109] offset:10240
	ds_write_b128 v1, v[110:113] offset:11264
	ds_write_b128 v1, v[114:117] offset:12288
	ds_write_b128 v1, v[118:121] offset:13312
	ds_write_b128 v1, v[2:5] offset:14336
	ds_write_b128 v1, v[6:9] offset:15360
	s_waitcnt lgkmcnt(0)
	s_barrier
	ds_read_b128 v[2:5], v194
	ds_read_b128 v[6:9], v194 offset:16384
	ds_read_b128 v[10:13], v194 offset:32768
	ds_read_b128 v[14:17], v194 offset:8192
	ds_read_b128 v[18:21], v194 offset:24576
	v_or_b32_e32 v1, 0x10000, v194
	s_lshl_b32 s2, s16, 3
	s_or_b32 s2, s2, s17
	s_waitcnt lgkmcnt(3)
	v_pk_add_f32 v[8:9], v[4:5], v[8:9]
	v_pk_add_f32 v[22:23], v[2:3], v[6:7]
	ds_read_b128 v[2:5], v194 offset:40960
	s_waitcnt lgkmcnt(3)
	v_pk_add_f32 v[26:27], v[8:9], v[12:13]
	ds_read_b128 v[6:9], v194 offset:49152
	v_pk_add_f32 v[28:29], v[22:23], v[10:11]
	ds_read_b128 v[10:13], v1
	ds_read_b128 v[22:25], v194 offset:57344
	v_or_b32_e32 v1, 0x14000, v194
	s_ashr_i32 s3, s2, 31
	s_waitcnt lgkmcnt(2)
	v_pk_add_f32 v[26:27], v[26:27], v[8:9]
	v_pk_add_f32 v[28:29], v[28:29], v[6:7]
	ds_read_b128 v[6:9], v1
	v_or_b32_e32 v1, 0x18000, v194
	s_waitcnt lgkmcnt(2)
	v_pk_add_f32 v[30:31], v[26:27], v[12:13]
	v_pk_add_f32 v[32:33], v[28:29], v[10:11]
	ds_read_b128 v[10:13], v1
	v_or_b32_e32 v1, 0x1c000, v194
	ds_read_b128 v[26:29], v1
	s_lshl_b64 s[2:3], s[2:3], 14
	s_waitcnt lgkmcnt(2)
	v_pk_add_f32 v[8:9], v[30:31], v[8:9]
	v_pk_add_f32 v[6:7], v[32:33], v[6:7]
	s_add_u32 s2, s12, s2
	s_waitcnt lgkmcnt(1)
	v_pk_add_f32 v[8:9], v[8:9], v[12:13]
	v_pk_add_f32 v[6:7], v[6:7], v[10:11]
	s_addc_u32 s3, s13, s3
	s_waitcnt lgkmcnt(0)
	v_pk_add_f32 v[8:9], v[8:9], v[28:29]
	v_pk_add_f32 v[6:7], v[6:7], v[26:27]
	global_store_dwordx4 v194, v[6:9], s[2:3] sc0 sc1
	v_or_b32_e32 v1, 0x12000, v194
	v_lshl_add_u64 v[26:27], s[2:3], 0, v[194:195]
	v_pk_add_f32 v[6:7], v[16:17], v[20:21]
	v_pk_add_f32 v[8:9], v[14:15], v[18:19]
	v_pk_add_f32 v[6:7], v[6:7], v[4:5]
	v_pk_add_f32 v[8:9], v[8:9], v[2:3]
	ds_read_b128 v[2:5], v1
	v_or_b32_e32 v1, 0x16000, v194
	v_pk_add_f32 v[10:11], v[6:7], v[24:25]
	v_pk_add_f32 v[12:13], v[8:9], v[22:23]
	ds_read_b128 v[6:9], v1
	v_or_b32_e32 v1, 0x1a000, v194
	s_waitcnt lgkmcnt(1)
	v_pk_add_f32 v[14:15], v[10:11], v[4:5]
	v_pk_add_f32 v[16:17], v[12:13], v[2:3]
	ds_read_b128 v[2:5], v1
	v_or_b32_e32 v1, 0x1e000, v194
	ds_read_b128 v[10:13], v1
	s_waitcnt lgkmcnt(2)
	v_pk_add_f32 v[6:7], v[16:17], v[6:7]
	v_pk_add_f32 v[8:9], v[14:15], v[8:9]
	s_waitcnt lgkmcnt(1)
	v_pk_add_f32 v[2:3], v[6:7], v[2:3]
	v_add_co_u32_e32 v6, vcc, 0x2000, v26
	v_pk_add_f32 v[4:5], v[8:9], v[4:5]
	s_nop 0
	v_addc_co_u32_e32 v7, vcc, 0, v27, vcc
	s_movk_i32 s2, 0x80
	s_waitcnt lgkmcnt(0)
	v_pk_add_f32 v[4:5], v[4:5], v[12:13]
	v_pk_add_f32 v[2:3], v[2:3], v[10:11]
	v_cmp_gt_u32_e32 vcc, s2, v0
	global_store_dwordx4 v[6:7], v[2:5], off sc0 sc1
	s_and_saveexec_b64 s[2:3], vcc
	s_cbranch_execz .LBB0_10
	v_lshlrev_b32_e32 v1, 2, v0
	v_or_b32_e32 v2, 0x20000, v1
	v_add_u32_e32 v3, 0x20200, v1
	v_add_u32_e32 v4, 0x20400, v1
	v_add_u32_e32 v5, 0x20600, v1
	v_or_b32_e32 v6, 0x20800, v1
	v_add_u32_e32 v7, 0x20a00, v1
	v_add_u32_e32 v8, 0x20c00, v1
	v_add_u32_e32 v9, 0x20e00, v1
	ds_read_b32 v2, v2
	ds_read_b32 v3, v3
	ds_read_b32 v4, v4
	ds_read_b32 v5, v5
	ds_read_b32 v6, v6
	ds_read_b32 v7, v7
	ds_read_b32 v8, v8
	ds_read_b32 v9, v9
	s_waitcnt lgkmcnt(7)
	v_add_f32_e32 v2, 0, v2
	s_waitcnt lgkmcnt(6)
	v_add_f32_e32 v2, v2, v3
	s_waitcnt lgkmcnt(5)
	v_add_f32_e32 v2, v2, v4
	s_waitcnt lgkmcnt(4)
	v_add_f32_e32 v2, v2, v5
	s_waitcnt lgkmcnt(3)
	v_add_f32_e32 v2, v2, v6
	s_waitcnt lgkmcnt(2)
	v_add_f32_e32 v2, v2, v7
	s_waitcnt lgkmcnt(1)
	v_add_f32_e32 v2, v2, v8
	s_waitcnt lgkmcnt(0)
	v_add_f32_e32 v2, v2, v9
	v_or_b32_e32 v3, 0x21000, v1
	v_add_u32_e32 v4, 0x21200, v1
	v_add_u32_e32 v5, 0x21400, v1
	v_add_u32_e32 v6, 0x21600, v1
	v_or_b32_e32 v7, 0x21800, v1
	v_add_u32_e32 v8, 0x21a00, v1
	v_add_u32_e32 v9, 0x21c00, v1
	v_add_u32_e32 v1, 0x21e00, v1
	ds_read_b32 v3, v3
	ds_read_b32 v4, v4
	ds_read_b32 v5, v5
	ds_read_b32 v6, v6
	ds_read_b32 v7, v7
	ds_read_b32 v8, v8
	ds_read_b32 v9, v9
	ds_read_b32 v1, v1
	s_waitcnt lgkmcnt(7)
	v_add_f32_e32 v2, v2, v3
	s_waitcnt lgkmcnt(6)
	v_add_f32_e32 v2, v2, v4
	s_waitcnt lgkmcnt(5)
	v_add_f32_e32 v2, v2, v5
	s_waitcnt lgkmcnt(0)
	v_add_f32_e32 v2, v2, v6
	v_add_f32_e32 v2, v2, v7
	s_lshl_b32 s2, s16, 10
	s_lshl_b32 s3, s17, 7
	v_add_f32_e32 v2, v2, v8
	s_or_b32 s2, s2, s3
	v_add_f32_e32 v2, v2, v9
	v_or_b32_e32 v0, s2, v0
	v_add_f32_e32 v2, v2, v1
	v_ashrrev_i32_e32 v1, 31, v0
	v_lshl_add_u64 v[0:1], v[0:1], 2, s[24:25]
	global_store_dword v[0:1], v2, off sc0 sc1
